# start-stagger spread widened: A8 unit 2x (max ~18 us), F2 unit 4x (max ~38 us); otherwise v040
# baseline (speedup 1.0000x reference)
.Lstg_a8_loop:
	s_sleep 40
	s_sub_u32 s8, s8, 1
	s_cmp_lg_u32 s8, 0
	s_cbranch_scc1 .Lstg_a8_loop

.Lstg_f2_loop:
	s_sleep 80
	s_sub_u32 s6, s6, 1
	s_cmp_lg_u32 s6, 0
	s_cbranch_scc1 .Lstg_f2_loop
